# the four selected/window branch-gate loads now go out before the overflow-flag exchange after the selected loop (no exposed gate-load latency left in a unit)
# speedup vs baseline: 1.0080x; 1.0026x over previous
; __device__ __forceinline__ bool attn_overflowed(const Softmax (&st)[2], const f32x4 (&O)[2][4]) {
;     float a = 0.f;
; #pragma unroll
;     for (int c = 0; c < 2; ++c) { a += fabsf(st[c].l[0]);
; #pragma unroll
;         for (int dt = 0; dt < 4; ++dt) a += (fabsf(O[c][dt][0]) + fabsf(O[c][dt][1])) + (fabsf(O[c][dt][2]) + fabsf(O[c][dt][3])); }
;     return !(a < 1e37f);
; }
; __device__ __forceinline__ void nsa_unit(unsigned char* ws, LAS unsigned char* lds, const LAS float* lut, int b, int g, int tau, int tid_in) {
;     ...
;         if (__any(attn_overflowed(st, O))) ovf[0] = 1u;
;         __syncthreads();
;         if (ovf[0] != 0u) {
.LBB0_1231:
	v_and_b32_e32 v61, 0x7fffffff, v70
	v_and_b32_e32 v60, 0x7fffffff, v66
	v_and_b32_e32 v77, 0x7fffffff, v71
	v_and_b32_e32 v76, 0x7fffffff, v67
	v_pk_add_f32 v[60:61], v[60:61], v[76:77]
	v_and_b32_e32 v77, 0x7fffffff, v72
	v_and_b32_e32 v76, 0x7fffffff, v68
	v_and_b32_e32 v79, 0x7fffffff, v73
	v_and_b32_e32 v78, 0x7fffffff, v69
	v_pk_add_f32 v[76:77], v[76:77], v[78:79]
	v_and_b32_e32 v79, 0x7fffffff, v65
	v_pk_add_f32 v[60:61], v[60:61], v[76:77]
	v_and_b32_e32 v77, 0x7fffffff, v64
	v_and_b32_e32 v76, 0x7fffffff, v63
	v_and_b32_e32 v78, 0x7fffffff, v62
	v_pk_add_f32 v[76:77], v[76:77], v[78:79]
	v_add_f32_e64 v59, |v74|, v61
	v_pk_add_f32 v[76:77], v[76:77], v[76:77] op_sel_hi:[0,1]
	v_add_f32_e32 v61, v60, v59
	v_add_f32_e64 v79, |v54|, |v55|
	v_add_f32_e64 v81, |v56|, |v57|
	v_and_b32_e32 v78, 0x7fffffff, v50
	v_and_b32_e32 v80, 0x7fffffff, v51
	v_and_b32_e32 v76, 0x7fffffff, v52
	v_and_b32_e32 v60, 0x7fffffff, v53
	v_pk_add_f32 v[78:79], v[78:79], v[80:81]
	v_pk_add_f32 v[60:61], v[76:77], v[60:61]
	v_and_b32_e32 v77, 0x7fffffff, v48
	v_pk_add_f32 v[60:61], v[78:79], v[60:61]
	v_and_b32_e32 v76, 0x7fffffff, v47
	v_and_b32_e32 v79, 0x7fffffff, v49
	v_and_b32_e32 v78, 0x7fffffff, v46
	v_pk_add_f32 v[76:77], v[76:77], v[78:79]
	v_add_f32_e64 v59, |v58|, v61
	v_pk_add_f32 v[76:77], v[76:77], v[76:77] op_sel_hi:[0,1]
	v_add_f32_e32 v61, v60, v59
	v_add_f32_e64 v79, |v42|, |v43|
	v_add_f32_e64 v81, |v44|, |v45|
	v_and_b32_e32 v78, 0x7fffffff, v38
	v_and_b32_e32 v80, 0x7fffffff, v39
	v_and_b32_e32 v76, 0x7fffffff, v40
	v_and_b32_e32 v60, 0x7fffffff, v41
	v_pk_add_f32 v[78:79], v[78:79], v[80:81]
	v_pk_add_f32 v[60:61], v[76:77], v[60:61]
	v_mad_u64_u32 v[168:169], s[10:11], v158, s0, 0
	v_pk_add_f32 v[60:61], v[78:79], v[60:61]
	v_mad_u64_u32 v[166:167], s[10:11], v4, s0, 0
	v_add_f32_e32 v59, v60, v61
	v_lshlrev_b32_e32 v174, 6, v191
	v_mad_i32_i24 v169, v159, s0, v169
	v_mad_i32_i24 v167, v5, s0, v167
	v_lshl_add_u64 v[244:245], s[30:31], 0, v[152:153]
	v_lshl_add_u64 v[250:251], v[244:245], 0, v[168:169]
	v_lshl_add_u64 v[242:243], v[244:245], 0, v[166:167]
	global_load_dword v250, v[250:251], off
	global_load_dword v242, v[242:243], off
	v_lshl_add_u64 v[244:245], s[40:41], 0, v[152:153]
	v_lshl_add_u64 v[246:247], v[244:245], 0, v[168:169]
	v_lshl_add_u64 v[248:249], v[244:245], 0, v[166:167]
	global_load_dword v246, v[246:247], off
	global_load_dword v248, v[248:249], off
	v_cmp_ngt_f32_e32 vcc, s54, v59
	s_cbranch_vccz .LBB0_1233
	v_mov_b32_e32 v59, s57
	ds_write_b32 v59, v177

; __device__ __forceinline__ void nsa_unit(unsigned char* ws, LAS unsigned char* lds, const LAS float* lut, int b, int g, int tau, int tid_in) {
;     ...
; #pragma unroll
;         for (int c = 0; c < 2; ++c) { const float sc = NSA_GATE(c, 1) / fmaxf(st[c].l[0], 1e-30f);
; #pragma unroll
;             for (int dt = 0; dt < 4; ++dt) resw[(c * 4 + dt) * 64] = resw[(c * 4 + dt) * 64] + O[c][dt] * sc; }
;     }
;     {
;         f32x4 O[2][4]; Softmax st[2];
; #pragma unroll
;         for (int c = 0; c < 2; ++c) { st[c].m = -1e30f; st[c].l = z4;
; #pragma unroll
;             for (int dt = 0; dt < 4; ++dt) O[c][dt] = z4; }
;         const unsigned char* kg = ws + WS_KW + ((size_t)b * SEQ * 256 + g * 64) * 2;
;         const unsigned char* vg = ws + WS_VWT + ((size_t)((b * 4 + g) * 64)) * SEQ * 2;
;         const int jlo = cur >= 8 ? cur - 8 : 0;
.LBB0_1296:
	s_waitcnt vmcnt(0)
	v_lshl_add_u64 v[34:35], s[30:31], 0, v[152:153]
	v_lshl_add_u64 v[30:31], v[34:35], 0, v[168:169]
	v_mov_b32_e32 v30, v250
	v_max_f32_e32 v31, v74, v74
	v_max_f32_e32 v31, 0xda24260, v31
	s_add_i32 s1, s37, -3
	s_cmp_le_i32 s50, s37
	s_cselect_b64 s[8:9], -1, 0
	s_cmp_gt_i32 s50, s37
	s_waitcnt vmcnt(0)
	v_div_scale_f32 v32, s[2:3], v31, v31, v30
	v_rcp_f32_e32 v33, v32
	s_nop 0
	v_fma_f32 v36, -v32, v33, 1.0
	v_fmac_f32_e32 v33, v36, v33
	v_div_scale_f32 v36, vcc, v30, v31, v30
	v_mul_f32_e32 v37, v36, v33
	v_fma_f32 v59, -v32, v37, v36
	v_fmac_f32_e32 v37, v59, v33
	v_fma_f32 v32, -v32, v37, v36
	v_div_fmas_f32 v32, v32, v33, v37
	v_div_fixup_f32 v36, v32, v31, v30
	s_waitcnt lgkmcnt(0)
	v_pk_fma_f32 v[212:213], v[72:73], v[36:37], v[212:213] op_sel_hi:[1,0,1]
	v_pk_fma_f32 v[210:211], v[70:71], v[36:37], v[210:211] op_sel_hi:[1,0,1]
	s_waitcnt lgkmcnt(0)
	v_pk_fma_f32 v[216:217], v[68:69], v[36:37], v[216:217] op_sel_hi:[1,0,1]
	v_pk_fma_f32 v[214:215], v[66:67], v[36:37], v[214:215] op_sel_hi:[1,0,1]
	s_waitcnt lgkmcnt(0)
	v_pk_fma_f32 v[220:221], v[64:65], v[36:37], v[220:221] op_sel_hi:[1,0,1]
	v_pk_fma_f32 v[218:219], v[62:63], v[36:37], v[218:219] op_sel_hi:[1,0,1]
	s_waitcnt lgkmcnt(0)
	v_pk_fma_f32 v[224:225], v[56:57], v[36:37], v[224:225] op_sel_hi:[1,0,1]
	v_pk_fma_f32 v[222:223], v[54:55], v[36:37], v[222:223] op_sel_hi:[1,0,1]
	v_lshl_add_u64 v[30:31], v[34:35], 0, v[166:167]
	v_max_f32_e32 v31, v58, v58
	v_max_f32_e32 v31, 0xda24260, v31
	s_waitcnt vmcnt(0)
	v_mov_b32_e32 v30, v242
	v_div_scale_f32 v32, s[2:3], v31, v31, v30
	v_rcp_f32_e32 v33, v32
	s_nop 0
	v_fma_f32 v34, -v32, v33, 1.0
	v_fmac_f32_e32 v33, v34, v33
	v_div_scale_f32 v34, vcc, v30, v31, v30
	v_mul_f32_e32 v35, v34, v33
	v_fma_f32 v36, -v32, v35, v34
	v_fmac_f32_e32 v35, v36, v33
	v_fma_f32 v32, -v32, v35, v34
	v_div_fmas_f32 v32, v32, v33, v35
	v_div_fixup_f32 v34, v32, v31, v30
	s_waitcnt lgkmcnt(0)
	v_pk_fma_f32 v[228:229], v[52:53], v[34:35], v[228:229] op_sel_hi:[1,0,1]
	v_pk_fma_f32 v[226:227], v[50:51], v[34:35], v[226:227] op_sel_hi:[1,0,1]
	s_waitcnt lgkmcnt(0)
	v_pk_fma_f32 v[232:233], v[48:49], v[34:35], v[232:233] op_sel_hi:[1,0,1]
	v_pk_fma_f32 v[230:231], v[46:47], v[34:35], v[230:231] op_sel_hi:[1,0,1]
	s_waitcnt lgkmcnt(0)
	v_pk_fma_f32 v[236:237], v[44:45], v[34:35], v[236:237] op_sel_hi:[1,0,1]
	v_pk_fma_f32 v[234:235], v[42:43], v[34:35], v[234:235] op_sel_hi:[1,0,1]
	s_waitcnt lgkmcnt(0)
	v_pk_fma_f32 v[238:239], v[38:39], v[34:35], v[238:239] op_sel_hi:[1,0,1]
	v_pk_fma_f32 v[240:241], v[40:41], v[34:35], v[240:241] op_sel_hi:[1,0,1]
	ds_write_b128 v188, v[26:29]
	ds_write_b128 v188, v[22:25] offset:32768
	s_waitcnt lgkmcnt(0)
	s_barrier
	s_cbranch_scc1 .LBB0_1322
	v_and_b32_e32 v30, 7, v185
	v_bitop3_b32 v30, v186, v30, 4 bitop3:0x36
	v_lshlrev_b32_e32 v175, 4, v30
	v_add_u32_e32 v30, s92, v184
	v_sub_u32_e32 v30, v30, v183
	s_lshl_b32 s3, s16, 6
	v_subrev_u32_e32 v30, s3, v30
	v_bitop3_b32 v31, v186, v185, 7 bitop3:0x78
	v_add_u32_e32 v191, 0x204, v30
	s_lshl_b32 s3, s16, 8
	v_lshlrev_b32_e32 v30, 4, v186
	v_lshlrev_b32_e32 v173, 4, v31
	v_add3_u32 v30, v190, s3, v30
	v_add_lshl_u32 v31, v184, v189, 2
	v_sub_u32_e32 v30, v30, v31
	s_lshl_b32 s3, s91, 5
	v_subrev_u32_e32 v30, s3, v30
	s_lshl_b32 s3, s37, 8
	v_subrev_u32_e32 v30, s3, v30
	v_readlane_b32 s3, v253, 56
	s_mov_b32 s17, s27
	s_add_i32 s2, s16, -6
	v_add_u32_e32 v192, s3, v30
	s_lshl_b64 s[6:7], s[16:17], 15
	v_readlane_b32 s3, v253, 49
	s_add_u32 s3, s3, s6
	v_readlane_b32 s5, v253, 50
	s_addc_u32 s5, s5, s7
	s_add_u32 s6, s3, s55
	v_lshl_add_u64 v[30:31], v[160:161], 0, v[156:157]
	s_addc_u32 s7, s5, s93
	v_lshl_add_u64 v[164:165], s[6:7], 0, v[30:31]
	s_lshl_b64 s[6:7], s[16:17], 7
	v_readlane_b32 s3, v253, 51
	v_lshl_add_u64 v[30:31], v[160:161], 0, s[18:19]
	s_add_u32 s6, s3, s6
	v_readlane_b32 s3, v253, 53
	v_lshl_add_u64 v[30:31], v[30:31], 0, v[162:163]
	s_addc_u32 s7, s3, s7
	v_mov_b32_e32 v32, v153
	v_mov_b32_e32 v33, v153
	v_lshl_add_u64 v[170:171], s[6:7], 0, v[30:31]
	v_mov_b32_e32 v30, v153
	v_mov_b32_e32 v31, v153
	v_mov_b64_e32 v[40:41], v[32:33]
	v_mov_b64_e32 v[44:45], v[32:33]
	v_mov_b64_e32 v[56:57], v[32:33]
	v_mov_b64_e32 v[36:37], v[32:33]
	v_mov_b64_e32 v[48:49], v[32:33]
	v_mov_b64_e32 v[52:53], v[32:33]
	v_mov_b64_e32 v[60:61], v[32:33]
	v_mov_b64_e32 v[64:65], v[32:33]
	v_mov_b64_e32 v[68:69], v[32:33]
	v_lshlrev_b32_e32 v172, 7, v187
	v_mov_b32_e32 v193, 0xf149f2ca
	s_mov_b32 s3, 0xffff0000
	s_mov_b32 s5, s16
	v_mov_b64_e32 v[38:39], v[30:31]
	v_mov_b64_e32 v[42:43], v[30:31]
	v_mov_b64_e32 v[54:55], v[30:31]
	v_mov_b64_e32 v[34:35], v[30:31]
	v_mov_b64_e32 v[46:47], v[30:31]
	v_mov_b64_e32 v[50:51], v[30:31]
	v_mov_b64_e32 v[58:59], v[30:31]
	v_mov_b64_e32 v[62:63], v[30:31]
	v_mov_b64_e32 v[66:67], v[30:31]
	v_mov_b32_e32 v197, 0xf149f2ca
